# attention: s_setprio 1 during the exp/PV (MFMA-dense) section of the tile loop, 0 elsewhere
# baseline (speedup 1.0000x reference)
; #define AT_TRR(dst, off) asm volatile("ds_read_b64_tr_b16 %0, %1 offset:%c2" : "=&v"(dst) : "v"(vaddr), "i"(off) : "memory")
; #define AT_PIN() do { _Pragma("unroll") for (int g_ = 0; g_ < 4; ++g_) { __builtin_amdgcn_sched_group_barrier(0x008, 1, 0); __builtin_amdgcn_sched_group_barrier(0x400, 2, 0); __builtin_amdgcn_sched_group_barrier(0x002, 2, 0); } \
;                 __builtin_amdgcn_sched_barrier(0); } while (0)
; __device__ __forceinline__ void attn_unit(const Frame& F, const bf16* __restrict__ proj, bf16* mix, const float* relb, const float* subg, int h, int qb, float lam, float one_m_li) {
;     ...
;             bf16x8 pb[4]; float lpart[4];
;     ...
;             AT_EXPBLK(0);
;             const unsigned vaddr = (unsigned)(uintptr_t)(lds + cur * STAGE + 16384 + (4 * hi + ((lane & 15) >> 2)) * 64 + ((lane >> 4) & 1) * 32 + (lane & 3) * 8);
;             s16x4 fl[2][4], fh[2][4];
;     ...
; #pragma unroll
;             for (int eb = 0; eb < 4; ++eb) { AT_TRR(fl[0][eb], eb * 4096); AT_TRR(fh[0][eb], eb * 4096 + 512); }
;     ...
;             AT_PVSTEP(0); AT_EXPBLK(1); AT_PIN();
;             AT_PVSTEP(1); AT_EXPBLK(2); AT_PIN();
;             AT_PVSTEP(2); AT_EXPBLK(3); AT_PIN();
;             AT_PVSTEP(3); __builtin_amdgcn_sched_barrier(0);
;             lsum += (lpart[0] + lpart[1]) + (lpart[2] + lpart[3]);
.LBB0_579:
	s_setprio 1
	v_exp_f32_e32 v169, v96
	v_add_u32_e32 v96, s79, v218
	v_add3_u32 v96, v96, v219, v220
	v_exp_f32_e32 v177, v99
	v_exp_f32_e32 v99, v102
	v_add3_u32 v102, v96, v221, s17
	ds_read_b64_tr_b16 v[182:183], v102 offset:0
	ds_read_b64_tr_b16 v[184:185], v102 offset:512
	ds_read_b64_tr_b16 v[236:237], v102 offset:4096
	ds_read_b64_tr_b16 v[238:239], v102 offset:4608
	ds_read_b64_tr_b16 v[240:241], v102 offset:8192
	ds_read_b64_tr_b16 v[242:243], v102 offset:8704
	ds_read_b64_tr_b16 v[244:245], v102 offset:12288
	ds_read_b64_tr_b16 v[246:247], v102 offset:12800
	ds_read_b64_tr_b16 v[248:249], v102 offset:1024
	ds_read_b64_tr_b16 v[250:251], v102 offset:1536
	ds_read_b64_tr_b16 v[228:229], v102 offset:5120
	ds_read_b64_tr_b16 v[230:231], v102 offset:5632
	ds_read_b64_tr_b16 v[196:197], v102 offset:9216
	ds_read_b64_tr_b16 v[198:199], v102 offset:9728
	ds_read_b64_tr_b16 v[200:201], v102 offset:13312
	v_exp_f32_e32 v97, v97
	v_exp_f32_e32 v175, v98
	v_exp_f32_e32 v171, v100
	v_exp_f32_e32 v173, v101
	v_exp_f32_e32 v101, v103
	ds_read_b64_tr_b16 v[202:203], v102 offset:13824
	s_waitcnt lgkmcnt(8)
	v_cvt_pk_bf16_f32 v178, v169, v97
	v_cvt_pk_bf16_f32 v179, v175, v177
	v_cvt_pk_bf16_f32 v180, v171, v173
	v_cvt_pk_bf16_f32 v181, v99, v101
	s_nop 1
	v_mfma_f32_32x32x16_bf16 v[48:63], v[182:185], v[178:181], v[48:63]
	v_exp_f32_e32 v103, v104
	v_exp_f32_e32 v105, v105
	v_mfma_f32_32x32x16_bf16 v[32:47], v[236:239], v[178:181], v[32:47]
	v_exp_f32_e32 v183, v106
	v_exp_f32_e32 v185, v107
	v_cvt_pk_bf16_f32 v236, v103, v105
	v_cvt_pk_bf16_f32 v237, v183, v185
	v_mfma_f32_32x32x16_bf16 v[16:31], v[240:243], v[178:181], v[16:31]
	v_exp_f32_e32 v107, v110
	v_mfma_f32_32x32x16_bf16 v[0:15], v[244:247], v[178:181], v[0:15]
	v_exp_f32_e32 v181, v109
	v_exp_f32_e32 v109, v111
	v_exp_f32_e32 v179, v108
	v_cvt_pk_bf16_f32 v239, v107, v109
	v_cvt_pk_bf16_f32 v238, v179, v181
	ds_read_b64_tr_b16 v[240:241], v102 offset:2048
	ds_read_b64_tr_b16 v[242:243], v102 offset:2560
	ds_read_b64_tr_b16 v[244:245], v102 offset:6144
	ds_read_b64_tr_b16 v[246:247], v102 offset:6656
	ds_read_b64_tr_b16 v[232:233], v102 offset:10240
	ds_read_b64_tr_b16 v[234:235], v102 offset:10752
	ds_read_b64_tr_b16 v[224:225], v102 offset:14336
	ds_read_b64_tr_b16 v[226:227], v102 offset:14848
	s_waitcnt lgkmcnt(8)
	s_nop 1
	v_mfma_f32_32x32x16_bf16 v[48:63], v[248:251], v[236:239], v[48:63]
	v_exp_f32_e32 v168, v80
	v_exp_f32_e32 v96, v81
	s_nop 0
	v_cvt_pk_bf16_f32 v80, v168, v96
	v_mfma_f32_32x32x16_bf16 v[32:47], v[228:231], v[236:239], v[32:47]
	v_exp_f32_e32 v174, v82
	v_exp_f32_e32 v176, v83
	s_nop 0
	v_cvt_pk_bf16_f32 v81, v174, v176
	v_mfma_f32_32x32x16_bf16 v[16:31], v[196:199], v[236:239], v[16:31]
	v_exp_f32_e32 v170, v84
	v_exp_f32_e32 v172, v85
	s_nop 0
	v_cvt_pk_bf16_f32 v82, v170, v172
	v_mfma_f32_32x32x16_bf16 v[0:15], v[200:203], v[236:239], v[0:15]
	v_exp_f32_e32 v98, v86
	v_exp_f32_e32 v100, v87
	s_nop 0
	v_cvt_pk_bf16_f32 v83, v98, v100
	ds_read_b64_tr_b16 v[84:85], v102 offset:3072
	ds_read_b64_tr_b16 v[86:87], v102 offset:3584
	ds_read_b64_tr_b16 v[196:197], v102 offset:7168
	ds_read_b64_tr_b16 v[198:199], v102 offset:7680
	ds_read_b64_tr_b16 v[200:201], v102 offset:11264
	ds_read_b64_tr_b16 v[202:203], v102 offset:11776
	ds_read_b64_tr_b16 v[228:229], v102 offset:15360
	ds_read_b64_tr_b16 v[230:231], v102 offset:15872
	s_waitcnt lgkmcnt(8)
	s_nop 1
	v_mfma_f32_32x32x16_bf16 v[48:63], v[240:243], v[80:83], v[48:63]
	v_exp_f32_e32 v102, v88
	v_exp_f32_e32 v104, v89
	s_nop 0
	v_cvt_pk_bf16_f32 v88, v102, v104
	v_mfma_f32_32x32x16_bf16 v[32:47], v[244:247], v[80:83], v[32:47]
	v_exp_f32_e32 v182, v90
	v_exp_f32_e32 v184, v91
	s_nop 0
	v_cvt_pk_bf16_f32 v89, v182, v184
	v_mfma_f32_32x32x16_bf16 v[16:31], v[232:235], v[80:83], v[16:31]
	v_exp_f32_e32 v178, v92
	v_exp_f32_e32 v180, v93
	s_nop 0
	v_cvt_pk_bf16_f32 v90, v178, v180
	v_mfma_f32_32x32x16_bf16 v[0:15], v[224:227], v[80:83], v[0:15]
	v_exp_f32_e32 v106, v94
	v_exp_f32_e32 v108, v95
	s_nop 0
	v_cvt_pk_bf16_f32 v91, v106, v108
	s_waitcnt lgkmcnt(0)
	s_nop 1
	v_mfma_f32_32x32x16_bf16 v[48:63], v[84:87], v[88:91], v[48:63]
	v_mfma_f32_32x32x16_bf16 v[32:47], v[196:199], v[88:91], v[32:47]
	v_mfma_f32_32x32x16_bf16 v[16:31], v[200:203], v[88:91], v[16:31]
	v_mfma_f32_32x32x16_bf16 v[0:15], v[228:231], v[88:91], v[0:15]
	v_add_f32_e64 v82, v170, v172
	v_add_f32_e64 v83, v171, v173
	v_add_f32_e64 v84, v98, v100
	v_add_f32_e64 v85, v99, v101
	v_add_f32_e64 v80, v174, v176
	v_add_f32_e64 v81, v175, v177
	v_pk_add_f32 v[82:83], v[82:83], v[84:85]
	v_pk_add_f32 v[84:85], v[168:169], v[96:97]
	v_pk_add_f32 v[86:87], v[106:107], v[108:109]
	v_pk_add_f32 v[80:81], v[84:85], v[80:81]
	v_pk_add_f32 v[84:85], v[178:179], v[180:181]
	v_pk_add_f32 v[80:81], v[80:81], v[82:83]
	v_pk_add_f32 v[82:83], v[182:183], v[184:185]
	v_pk_add_f32 v[84:85], v[84:85], v[86:87]
	v_pk_add_f32 v[86:87], v[102:103], v[104:105]
	s_nop 0
	v_pk_add_f32 v[82:83], v[86:87], v[82:83]
	s_nop 0
	v_pk_add_f32 v[82:83], v[82:83], v[84:85]
	s_nop 0
	v_pk_add_f32 v[80:81], v[80:81], v[82:83]
	s_nop 0
	v_add_f32_e32 v80, v80, v81
	v_add_f32_e32 v163, v163, v80
.LBB0_580:
	s_setprio 0
	s_addk_i32 s60, 0x100
	s_add_i32 s73, s73, 0x8000
	s_add_i32 s13, s13, 1
	v_lshl_add_u64 v[164:165], v[164:165], 0, s[68:69]
	s_cmp_eq_u32 s15, s60
	v_lshl_add_u64 v[166:167], v[166:167], 0, s[68:69]
	s_waitcnt lgkmcnt(0)
	s_barrier
	s_cbranch_scc1 .LBB0_592
